# speedup vs baseline: 1.0212x; 1.0205x over previous
_Z11gemm_kernelILi256ELi192ELi4ELi2ELi4ELi2ELi2ELi0EEvPKDF16_S1_iiiPDF16_PfPK15HIP_vector_typeIfLj2EE:
	s_load_dwordx8 s[4:11], s[0:1], 0x0
	s_load_dwordx2 s[12:13], s[0:1], 0x30
	s_lshr_b32 s18, s2, 3
	v_readfirstlane_b32 s17, v0
	s_lshr_b32 s14, s17, 6
	s_waitcnt lgkmcnt(0)
	s_ashr_i32 s11, s8, 31
	s_lshr_b32 s3, s11, 22
	s_add_i32 s3, s8, s3
	s_ashr_i32 s15, s3, 10
	s_abs_i32 s16, s15
	v_cvt_f32_u32_e32 v1, s16
	s_sub_i32 s21, 0, s16
	s_mul_hi_i32 s19, s9, 0x2aaaaaab
	s_lshr_b32 s20, s19, 31
	v_rcp_iflag_f32_e32 v1, v1
	s_ashr_i32 s19, s19, 6
	s_add_i32 s19, s19, s20
	s_bfe_u32 s20, s2, 0x20001
	v_mul_f32_e32 v1, 0x4f7ffffe, v1
	v_cvt_u32_f32_e32 v1, v1
	s_ashr_i32 s3, s3, 31
	s_mul_i32 s20, s15, s20
	v_mov_b32_e32 v97, 0
	v_readfirstlane_b32 s22, v1
	s_mul_i32 s21, s21, s22
	s_mul_hi_u32 s21, s22, s21
	s_add_i32 s22, s22, s21
	s_mul_hi_u32 s22, s18, s22
	s_mul_i32 s21, s22, s16
	s_sub_i32 s23, s18, s21
	s_add_i32 s24, s22, 1
	s_sub_i32 s25, s23, s16
	s_cmp_ge_u32 s23, s16
	s_cselect_b32 s22, s24, s22
	s_cselect_b32 s23, s25, s23
	s_add_i32 s24, s22, 1
	s_cmp_ge_u32 s23, s16
	s_cselect_b32 s16, s24, s22
	s_xor_b32 s16, s16, s3
	s_sub_i32 s3, s16, s3
	s_mul_i32 s15, s3, s15
	s_sub_i32 s15, s18, s15
	s_add_i32 s15, s15, s20
	s_bitcmp1_b32 s2, 0
	v_bfe_u32 v1, v0, 3, 3
	s_cselect_b32 s2, s19, 0
	v_lshl_or_b32 v1, s14, 3, v1
	s_add_i32 s18, s3, s2
	s_lshl_b32 s19, s15, 8
	v_lshrrev_b32_e32 v2, 1, v1
	s_lshl_b32 s2, s14, 10
	v_xor_b32_e32 v6, v2, v0
	v_add_u32_e32 v2, s19, v1
	s_cmp_lg_u32 0, -1
	s_mul_i32 s15, s18, 0xc0
	v_ashrrev_i32_e32 v3, 31, v2
	s_cselect_b32 s3, 0, 0
	v_lshlrev_b64 v[2:3], 7, v[2:3]
	v_add_u32_e32 v4, s15, v1
	s_add_i32 s22, s2, s3
	v_lshlrev_b32_e32 v1, 4, v6
	s_lshr_b32 s3, s17, 1
	v_lshl_add_u64 v[2:3], s[4:5], 0, v[2:3]
	v_ashrrev_i32_e32 v5, 31, v4
	v_and_b32_e32 v96, 0x70, v1
	s_add_i32 s24, s22, 0x8000
	s_and_b32 s20, s3, 0x7fffffc0
	v_lshlrev_b64 v[4:5], 7, v[4:5]
	v_lshl_add_u64 v[104:105], v[2:3], 0, v[96:97]
	s_bitcmp1_b32 s17, 6
	s_mov_b64 s[4:5], 0x2000
	s_mov_b32 m0, s22
	s_nop 0
	global_load_lds_dwordx4 v[104:105], off
	v_lshl_add_u64 v[4:5], s[6:7], 0, v[4:5]
	s_cselect_b32 s16, 0x60, 0
	v_lshl_add_u64 v[110:111], v[104:105], 0, s[4:5]
	s_mov_b64 s[6:7], 0x4000
	s_add_i32 s3, s22, 0x2000
	s_mov_b32 m0, s3
	s_nop 0
	global_load_lds_dwordx4 v[110:111], off
	v_lshl_add_u64 v[108:109], v[104:105], 0, s[6:7]
	s_mov_b64 s[26:27], 0x6000
	s_add_i32 s3, s22, 0x4000
	s_mov_b32 m0, s3
	s_nop 0
	global_load_lds_dwordx4 v[108:109], off
	v_lshl_add_u64 v[106:107], v[104:105], 0, s[26:27]
	s_add_i32 s3, s22, 0x6000
	s_mov_b32 m0, s3
	s_nop 0
	global_load_lds_dwordx4 v[106:107], off
	v_lshl_add_u64 v[98:99], v[4:5], 0, v[96:97]
	s_mov_b32 m0, s24
	s_nop 0
	global_load_lds_dwordx4 v[98:99], off
	v_lshl_add_u64 v[100:101], v[98:99], 0, s[4:5]
	s_add_i32 s3, s22, 0xa000
	s_mov_b32 m0, s3
	s_nop 0
	global_load_lds_dwordx4 v[100:101], off
	v_lshl_add_u64 v[102:103], v[98:99], 0, s[6:7]
	s_add_i32 s3, s22, 0xc000
	s_mov_b32 m0, s3
	s_nop 0
	global_load_lds_dwordx4 v[102:103], off
	s_mov_b32 s21, 1
	s_mov_b32 s23, 0
	s_cmp_lt_i32 s10, 64
	v_mov_b32_e32 v96, v97
	v_mov_b32_e32 v95, v97
	v_mov_b32_e32 v94, v97
	v_mov_b32_e32 v93, v97
	v_mov_b32_e32 v92, v97
	v_mov_b32_e32 v91, v97
	v_mov_b32_e32 v90, v97
	v_mov_b32_e32 v89, v97
	v_mov_b32_e32 v88, v97
	v_mov_b32_e32 v87, v97
	v_mov_b32_e32 v86, v97
	v_mov_b32_e32 v85, v97
	v_mov_b32_e32 v84, v97
	v_mov_b32_e32 v83, v97
	v_mov_b32_e32 v82, v97
	v_mov_b32_e32 v81, v97
	v_mov_b32_e32 v80, v97
	v_mov_b32_e32 v79, v97
	v_mov_b32_e32 v78, v97
	v_mov_b32_e32 v77, v97
	v_mov_b32_e32 v76, v97
	v_mov_b32_e32 v75, v97
	v_mov_b32_e32 v74, v97
	v_mov_b32_e32 v73, v97
	v_mov_b32_e32 v72, v97
	v_mov_b32_e32 v71, v97
	v_mov_b32_e32 v70, v97
	v_mov_b32_e32 v69, v97
	v_mov_b32_e32 v68, v97
	v_mov_b32_e32 v67, v97
	v_mov_b32_e32 v66, v97
	v_mov_b32_e32 v65, v97
	v_mov_b32_e32 v64, v97
	v_mov_b32_e32 v63, v97
	v_mov_b32_e32 v62, v97
	v_mov_b32_e32 v61, v97
	v_mov_b32_e32 v60, v97
	v_mov_b32_e32 v59, v97
	v_mov_b32_e32 v58, v97
	v_mov_b32_e32 v57, v97
	v_mov_b32_e32 v56, v97
	v_mov_b32_e32 v55, v97
	v_mov_b32_e32 v54, v97
	v_mov_b32_e32 v53, v97
	v_mov_b32_e32 v52, v97
	v_mov_b32_e32 v51, v97
	v_mov_b32_e32 v50, v97
	v_mov_b32_e32 v49, v97
	v_mov_b32_e32 v48, v97
	v_mov_b32_e32 v47, v97
	v_mov_b32_e32 v46, v97
	v_mov_b32_e32 v45, v97
	v_mov_b32_e32 v44, v97
	v_mov_b32_e32 v43, v97
	v_mov_b32_e32 v42, v97
	v_mov_b32_e32 v41, v97
	v_mov_b32_e32 v40, v97
	v_mov_b32_e32 v39, v97
	v_mov_b32_e32 v38, v97
	v_mov_b32_e32 v37, v97
	v_mov_b32_e32 v36, v97
	v_mov_b32_e32 v35, v97
	v_mov_b32_e32 v34, v97
	v_mov_b32_e32 v33, v97
	v_mov_b32_e32 v32, v97
	v_mov_b32_e32 v31, v97
	v_mov_b32_e32 v30, v97
	v_mov_b32_e32 v29, v97
	v_mov_b32_e32 v28, v97
	v_mov_b32_e32 v27, v97
	v_mov_b32_e32 v26, v97
	v_mov_b32_e32 v25, v97
	v_mov_b32_e32 v24, v97
	v_mov_b32_e32 v23, v97
	v_mov_b32_e32 v22, v97
	v_mov_b32_e32 v21, v97
	v_mov_b32_e32 v20, v97
	v_mov_b32_e32 v19, v97
	v_mov_b32_e32 v18, v97
	v_mov_b32_e32 v17, v97
	v_mov_b32_e32 v16, v97
	v_mov_b32_e32 v15, v97
	v_mov_b32_e32 v14, v97
	v_mov_b32_e32 v13, v97
	v_mov_b32_e32 v12, v97
	v_mov_b32_e32 v11, v97
	v_mov_b32_e32 v10, v97
	v_mov_b32_e32 v9, v97
	v_mov_b32_e32 v8, v97
	v_mov_b32_e32 v7, v97
	v_mov_b32_e32 v6, v97
	v_mov_b32_e32 v5, v97
	v_mov_b32_e32 v4, v97
	v_mov_b32_e32 v3, v97
	v_mov_b32_e32 v2, v97
	v_and_b32_e32 v162, 31, v0
	v_bfe_u32 v1, v0, 5, 1
	s_cbranch_scc1 .LBB2_6
	s_ashr_i32 s3, s10, 31
	s_lshr_b32 s3, s3, 26
	s_add_i32 s3, s10, s3
	v_lshrrev_b32_e32 v2, 1, v0
	s_ashr_i32 s25, s3, 6
	v_bitop3_b32 v2, v1, v2, 7 bitop3:0x78
	s_cmp_lg_u32 0, -1
	v_lshlrev_b32_e32 v120, 4, v2
	v_or_b32_e32 v2, s20, v162
	s_cselect_b32 s3, 0, 0
	v_lshl_add_u32 v121, v2, 7, 0
	v_or_b32_e32 v2, s16, v162
	s_mov_b32 s10, s8
	s_add_i32 s8, s3, s2
	s_ashr_i32 s3, s9, 31
	s_mov_b32 s2, s9
	v_lshl_add_u32 v122, v2, 7, 0
	s_lshl_b64 s[2:3], s[2:3], 7
	v_mov_b32_e32 v2, 0
	s_addk_i32 s8, 0x6000
	v_xor_b32_e32 v123, 32, v120
	v_xor_b32_e32 v124, 64, v120
	v_xor_b32_e32 v125, 0x60, v120
	s_lshl_b64 s[4:5], s[10:11], 7
	s_mov_b64 s[6:7], s[2:3]
	s_mov_b32 s9, 0
	v_mov_b32_e32 v3, v2
	v_mov_b32_e32 v4, v2
	v_mov_b32_e32 v5, v2
	v_mov_b32_e32 v6, v2
	v_mov_b32_e32 v7, v2
	v_mov_b32_e32 v8, v2
	v_mov_b32_e32 v9, v2
	v_mov_b32_e32 v10, v2
	v_mov_b32_e32 v11, v2
	v_mov_b32_e32 v12, v2
	v_mov_b32_e32 v13, v2
	v_mov_b32_e32 v14, v2
	v_mov_b32_e32 v15, v2
	v_mov_b32_e32 v16, v2
	v_mov_b32_e32 v17, v2
	v_mov_b32_e32 v18, v2
	v_mov_b32_e32 v19, v2
	v_mov_b32_e32 v20, v2
	v_mov_b32_e32 v21, v2
	v_mov_b32_e32 v22, v2
	v_mov_b32_e32 v23, v2
	v_mov_b32_e32 v24, v2
	v_mov_b32_e32 v25, v2
	v_mov_b32_e32 v26, v2
	v_mov_b32_e32 v27, v2
	v_mov_b32_e32 v28, v2
	v_mov_b32_e32 v29, v2
	v_mov_b32_e32 v30, v2
	v_mov_b32_e32 v31, v2
	v_mov_b32_e32 v32, v2
	v_mov_b32_e32 v33, v2
	v_mov_b32_e32 v34, v2
	v_mov_b32_e32 v35, v2
	v_mov_b32_e32 v36, v2
	v_mov_b32_e32 v37, v2
	v_mov_b32_e32 v38, v2
	v_mov_b32_e32 v39, v2
	v_mov_b32_e32 v40, v2
	v_mov_b32_e32 v41, v2
	v_mov_b32_e32 v42, v2
	v_mov_b32_e32 v43, v2
	v_mov_b32_e32 v44, v2
	v_mov_b32_e32 v45, v2
	v_mov_b32_e32 v46, v2
	v_mov_b32_e32 v47, v2
	v_mov_b32_e32 v48, v2
	v_mov_b32_e32 v49, v2
	v_mov_b32_e32 v50, v2
	v_mov_b32_e32 v51, v2
	v_mov_b32_e32 v52, v2
	v_mov_b32_e32 v53, v2
	v_mov_b32_e32 v54, v2
	v_mov_b32_e32 v55, v2
	v_mov_b32_e32 v56, v2
	v_mov_b32_e32 v57, v2
	v_mov_b32_e32 v58, v2
	v_mov_b32_e32 v59, v2
	v_mov_b32_e32 v60, v2
	v_mov_b32_e32 v61, v2
	v_mov_b32_e32 v62, v2
	v_mov_b32_e32 v63, v2
	v_mov_b32_e32 v64, v2
	v_mov_b32_e32 v65, v2
	v_mov_b32_e32 v66, v2
	v_mov_b32_e32 v67, v2
	v_mov_b32_e32 v68, v2
	v_mov_b32_e32 v69, v2
	v_mov_b32_e32 v70, v2
	v_mov_b32_e32 v71, v2
	v_mov_b32_e32 v72, v2
	v_mov_b32_e32 v73, v2
	v_mov_b32_e32 v74, v2
	v_mov_b32_e32 v75, v2
	v_mov_b32_e32 v76, v2
	v_mov_b32_e32 v77, v2
	v_mov_b32_e32 v78, v2
	v_mov_b32_e32 v79, v2
	v_mov_b32_e32 v80, v2
	v_mov_b32_e32 v81, v2
	v_mov_b32_e32 v82, v2
	v_mov_b32_e32 v83, v2
	v_mov_b32_e32 v84, v2
	v_mov_b32_e32 v85, v2
	v_mov_b32_e32 v86, v2
	v_mov_b32_e32 v87, v2
	v_mov_b32_e32 v88, v2
	v_mov_b32_e32 v89, v2
	v_mov_b32_e32 v90, v2
	v_mov_b32_e32 v91, v2
	v_mov_b32_e32 v92, v2
	v_mov_b32_e32 v93, v2
	v_mov_b32_e32 v94, v2
	v_mov_b32_e32 v95, v2
	v_mov_b32_e32 v96, v2
	v_mov_b32_e32 v97, v2
	v_lshl_add_u64 v[190:191], v[104:105], 0, s[4:5]
	v_lshl_add_u64 v[192:193], v[110:111], 0, s[4:5]
	v_lshl_add_u64 v[194:195], v[108:109], 0, s[4:5]
	v_lshl_add_u64 v[196:197], v[106:107], 0, s[4:5]
	v_lshl_add_u64 v[198:199], v[98:99], 0, s[2:3]
	v_lshl_add_u64 v[200:201], v[100:101], 0, s[2:3]
	v_lshl_add_u64 v[202:203], v[102:103], 0, s[2:3]
	v_and_b32_e32 v184, 15, v0
	v_bfe_u32 v185, v0, 4, 2
	v_lshrrev_b32_e32 v186, 1, v184
	v_xor_b32_e32 v186, v185, v186
	v_lshlrev_b32_e32 v182, 4, v186
	v_xor_b32_e32 v183, 64, v182
	v_add_u32_e32 v180, s20, v184
	v_lshlrev_b32_e32 v180, 7, v180
	v_add_u32_e32 v181, s16, v184
	v_lshlrev_b32_e32 v181, 7, v181
	v_add_u32_e32 v181, 0x8000, v181
	s_add_i32 s25, s25, -1
.Lqkv_loop:
	s_waitcnt vmcnt(0)
	s_barrier
	s_mul_i32 s10, s23, 0xe000
	s_mul_i32 s11, s21, 0xe000
	v_add_u32_e32 v184, s10, v180
	v_add_u32_e32 v185, s10, v181
	s_add_i32 s11, s11, s22
	s_xor_b32 s23, s23, 1
	s_xor_b32 s21, s21, 1
	v_add_u32_e32 v186, v184, v182
	v_add_u32_e32 v187, v185, v182
	ds_read_b128 v[100:103], v186
	ds_read_b128 v[116:119], v187
	ds_read_b128 v[120:123], v187 offset:2048
	ds_read_b128 v[124:127], v187 offset:4096
	ds_read_b128 v[128:131], v187 offset:6144
	ds_read_b128 v[132:135], v187 offset:8192
	ds_read_b128 v[136:139], v187 offset:10240
	ds_read_b128 v[104:107], v186 offset:2048
	ds_read_b128 v[108:111], v186 offset:4096
	ds_read_b128 v[112:115], v186 offset:6144
	s_mov_b32 m0, s11
	s_nop 0
	global_load_lds_dwordx4 v[190:191], off
	v_lshl_add_u64 v[190:191], v[190:191], 0, s[4:5]
	s_add_i32 m0, s11, 0x2000
	s_nop 0
	global_load_lds_dwordx4 v[192:193], off
	v_lshl_add_u64 v[192:193], v[192:193], 0, s[4:5]
	s_waitcnt lgkmcnt(8)
	s_add_i32 m0, s11, 0x4000
	v_mfma_f32_16x16x32_f16 v[2:5], v[116:119], v[100:103], v[2:5]
	global_load_lds_dwordx4 v[194:195], off
	v_lshl_add_u64 v[194:195], v[194:195], 0, s[4:5]
	s_waitcnt lgkmcnt(7)
	v_mfma_f32_16x16x32_f16 v[6:9], v[120:123], v[100:103], v[6:9]
	s_waitcnt lgkmcnt(6)
	v_mfma_f32_16x16x32_f16 v[10:13], v[124:127], v[100:103], v[10:13]
	s_waitcnt lgkmcnt(5)
	v_mfma_f32_16x16x32_f16 v[14:17], v[128:131], v[100:103], v[14:17]
	s_waitcnt lgkmcnt(4)
	s_add_i32 m0, s11, 0x6000
	v_mfma_f32_16x16x32_f16 v[18:21], v[132:135], v[100:103], v[18:21]
	global_load_lds_dwordx4 v[196:197], off
	v_lshl_add_u64 v[196:197], v[196:197], 0, s[4:5]
	s_waitcnt lgkmcnt(3)
	v_mfma_f32_16x16x32_f16 v[22:25], v[136:139], v[100:103], v[22:25]
	v_add_u32_e32 v188, v184, v183
	v_add_u32_e32 v189, v185, v183
	ds_read_b128 v[140:143], v188
	ds_read_b128 v[156:159], v189
	ds_read_b128 v[160:163], v189 offset:2048
	ds_read_b128 v[164:167], v189 offset:4096
	ds_read_b128 v[168:171], v189 offset:6144
	ds_read_b128 v[172:175], v189 offset:8192
	ds_read_b128 v[176:179], v189 offset:10240
	ds_read_b128 v[144:147], v188 offset:2048
	ds_read_b128 v[148:151], v188 offset:4096
	ds_read_b128 v[152:155], v188 offset:6144
	s_waitcnt lgkmcnt(12)
	v_mfma_f32_16x16x32_f16 v[26:29], v[116:119], v[104:107], v[26:29]
	v_mfma_f32_16x16x32_f16 v[30:33], v[120:123], v[104:107], v[30:33]
	s_add_i32 m0, s11, 0x8000
	v_mfma_f32_16x16x32_f16 v[34:37], v[124:127], v[104:107], v[34:37]
	global_load_lds_dwordx4 v[198:199], off
	v_lshl_add_u64 v[198:199], v[198:199], 0, s[2:3]
	v_mfma_f32_16x16x32_f16 v[38:41], v[128:131], v[104:107], v[38:41]
	v_mfma_f32_16x16x32_f16 v[42:45], v[132:135], v[104:107], v[42:45]
	v_mfma_f32_16x16x32_f16 v[46:49], v[136:139], v[104:107], v[46:49]
	s_waitcnt lgkmcnt(11)
	s_add_i32 m0, s11, 0xa000
	v_mfma_f32_16x16x32_f16 v[50:53], v[116:119], v[108:111], v[50:53]
	global_load_lds_dwordx4 v[200:201], off
	v_lshl_add_u64 v[200:201], v[200:201], 0, s[2:3]
	v_mfma_f32_16x16x32_f16 v[54:57], v[120:123], v[108:111], v[54:57]
	v_mfma_f32_16x16x32_f16 v[58:61], v[124:127], v[108:111], v[58:61]
	v_mfma_f32_16x16x32_f16 v[62:65], v[128:131], v[108:111], v[62:65]
	s_add_i32 m0, s11, 0xc000
	v_mfma_f32_16x16x32_f16 v[66:69], v[132:135], v[108:111], v[66:69]
	global_load_lds_dwordx4 v[202:203], off
	v_lshl_add_u64 v[202:203], v[202:203], 0, s[2:3]
	v_mfma_f32_16x16x32_f16 v[70:73], v[136:139], v[108:111], v[70:73]
	s_waitcnt lgkmcnt(10)
	v_mfma_f32_16x16x32_f16 v[74:77], v[116:119], v[112:115], v[74:77]
	v_mfma_f32_16x16x32_f16 v[78:81], v[120:123], v[112:115], v[78:81]
	v_mfma_f32_16x16x32_f16 v[82:85], v[124:127], v[112:115], v[82:85]
	v_mfma_f32_16x16x32_f16 v[86:89], v[128:131], v[112:115], v[86:89]
	v_mfma_f32_16x16x32_f16 v[90:93], v[132:135], v[112:115], v[90:93]
	v_mfma_f32_16x16x32_f16 v[94:97], v[136:139], v[112:115], v[94:97]
	s_waitcnt lgkmcnt(8)
	v_mfma_f32_16x16x32_f16 v[2:5], v[156:159], v[140:143], v[2:5]
	s_waitcnt lgkmcnt(7)
	v_mfma_f32_16x16x32_f16 v[6:9], v[160:163], v[140:143], v[6:9]
	s_waitcnt lgkmcnt(6)
	v_mfma_f32_16x16x32_f16 v[10:13], v[164:167], v[140:143], v[10:13]
	s_waitcnt lgkmcnt(5)
	v_mfma_f32_16x16x32_f16 v[14:17], v[168:171], v[140:143], v[14:17]
	s_waitcnt lgkmcnt(4)
	v_mfma_f32_16x16x32_f16 v[18:21], v[172:175], v[140:143], v[18:21]
	s_waitcnt lgkmcnt(3)
	v_mfma_f32_16x16x32_f16 v[22:25], v[176:179], v[140:143], v[22:25]
	s_waitcnt lgkmcnt(2)
	v_mfma_f32_16x16x32_f16 v[26:29], v[156:159], v[144:147], v[26:29]
	v_mfma_f32_16x16x32_f16 v[30:33], v[160:163], v[144:147], v[30:33]
	v_mfma_f32_16x16x32_f16 v[34:37], v[164:167], v[144:147], v[34:37]
	v_mfma_f32_16x16x32_f16 v[38:41], v[168:171], v[144:147], v[38:41]
	v_mfma_f32_16x16x32_f16 v[42:45], v[172:175], v[144:147], v[42:45]
	v_mfma_f32_16x16x32_f16 v[46:49], v[176:179], v[144:147], v[46:49]
	s_waitcnt lgkmcnt(1)
	v_mfma_f32_16x16x32_f16 v[50:53], v[156:159], v[148:151], v[50:53]
	v_mfma_f32_16x16x32_f16 v[54:57], v[160:163], v[148:151], v[54:57]
	v_mfma_f32_16x16x32_f16 v[58:61], v[164:167], v[148:151], v[58:61]
	v_mfma_f32_16x16x32_f16 v[62:65], v[168:171], v[148:151], v[62:65]
	v_mfma_f32_16x16x32_f16 v[66:69], v[172:175], v[148:151], v[66:69]
	v_mfma_f32_16x16x32_f16 v[70:73], v[176:179], v[148:151], v[70:73]
	s_waitcnt lgkmcnt(0)
	v_mfma_f32_16x16x32_f16 v[74:77], v[156:159], v[152:155], v[74:77]
	v_mfma_f32_16x16x32_f16 v[78:81], v[160:163], v[152:155], v[78:81]
	v_mfma_f32_16x16x32_f16 v[82:85], v[164:167], v[152:155], v[82:85]
	v_mfma_f32_16x16x32_f16 v[86:89], v[168:171], v[152:155], v[86:89]
	v_mfma_f32_16x16x32_f16 v[90:93], v[172:175], v[152:155], v[90:93]
	v_mfma_f32_16x16x32_f16 v[94:97], v[176:179], v[152:155], v[94:97]
	s_add_i32 s9, s9, 1
	s_cmp_lt_i32 s9, s25
	s_cbranch_scc1 .Lqkv_loop
	s_waitcnt vmcnt(0)
	s_barrier
	s_mul_i32 s10, s23, 0xe000
	v_add_u32_e32 v184, s10, v180
	v_add_u32_e32 v185, s10, v181
	s_xor_b32 s23, s23, 1
	s_xor_b32 s21, s21, 1
	v_add_u32_e32 v186, v184, v182
	v_add_u32_e32 v187, v185, v182
	ds_read_b128 v[100:103], v186
	ds_read_b128 v[116:119], v187
	ds_read_b128 v[120:123], v187 offset:2048
	ds_read_b128 v[124:127], v187 offset:4096
	ds_read_b128 v[128:131], v187 offset:6144
	ds_read_b128 v[132:135], v187 offset:8192
	ds_read_b128 v[136:139], v187 offset:10240
	ds_read_b128 v[104:107], v186 offset:2048
	ds_read_b128 v[108:111], v186 offset:4096
	ds_read_b128 v[112:115], v186 offset:6144
	s_waitcnt lgkmcnt(8)
	v_mfma_f32_16x16x32_f16 v[2:5], v[116:119], v[100:103], v[2:5]
	s_waitcnt lgkmcnt(7)
	v_mfma_f32_16x16x32_f16 v[6:9], v[120:123], v[100:103], v[6:9]
	s_waitcnt lgkmcnt(6)
	v_mfma_f32_16x16x32_f16 v[10:13], v[124:127], v[100:103], v[10:13]
	s_waitcnt lgkmcnt(5)
	v_mfma_f32_16x16x32_f16 v[14:17], v[128:131], v[100:103], v[14:17]
	s_waitcnt lgkmcnt(4)
	v_mfma_f32_16x16x32_f16 v[18:21], v[132:135], v[100:103], v[18:21]
	s_waitcnt lgkmcnt(3)
	v_mfma_f32_16x16x32_f16 v[22:25], v[136:139], v[100:103], v[22:25]
	v_add_u32_e32 v188, v184, v183
	v_add_u32_e32 v189, v185, v183
	ds_read_b128 v[140:143], v188
	ds_read_b128 v[156:159], v189
	ds_read_b128 v[160:163], v189 offset:2048
	ds_read_b128 v[164:167], v189 offset:4096
	ds_read_b128 v[168:171], v189 offset:6144
	ds_read_b128 v[172:175], v189 offset:8192
	ds_read_b128 v[176:179], v189 offset:10240
	ds_read_b128 v[144:147], v188 offset:2048
	ds_read_b128 v[148:151], v188 offset:4096
	ds_read_b128 v[152:155], v188 offset:6144
	s_waitcnt lgkmcnt(12)
	v_mfma_f32_16x16x32_f16 v[26:29], v[116:119], v[104:107], v[26:29]
	v_mfma_f32_16x16x32_f16 v[30:33], v[120:123], v[104:107], v[30:33]
	v_mfma_f32_16x16x32_f16 v[34:37], v[124:127], v[104:107], v[34:37]
	v_mfma_f32_16x16x32_f16 v[38:41], v[128:131], v[104:107], v[38:41]
	v_mfma_f32_16x16x32_f16 v[42:45], v[132:135], v[104:107], v[42:45]
	v_mfma_f32_16x16x32_f16 v[46:49], v[136:139], v[104:107], v[46:49]
	s_waitcnt lgkmcnt(11)
	v_mfma_f32_16x16x32_f16 v[50:53], v[116:119], v[108:111], v[50:53]
	v_mfma_f32_16x16x32_f16 v[54:57], v[120:123], v[108:111], v[54:57]
	v_mfma_f32_16x16x32_f16 v[58:61], v[124:127], v[108:111], v[58:61]
	v_mfma_f32_16x16x32_f16 v[62:65], v[128:131], v[108:111], v[62:65]
	v_mfma_f32_16x16x32_f16 v[66:69], v[132:135], v[108:111], v[66:69]
	v_mfma_f32_16x16x32_f16 v[70:73], v[136:139], v[108:111], v[70:73]
	s_waitcnt lgkmcnt(10)
	v_mfma_f32_16x16x32_f16 v[74:77], v[116:119], v[112:115], v[74:77]
	v_mfma_f32_16x16x32_f16 v[78:81], v[120:123], v[112:115], v[78:81]
	v_mfma_f32_16x16x32_f16 v[82:85], v[124:127], v[112:115], v[82:85]
	v_mfma_f32_16x16x32_f16 v[86:89], v[128:131], v[112:115], v[86:89]
	v_mfma_f32_16x16x32_f16 v[90:93], v[132:135], v[112:115], v[90:93]
	v_mfma_f32_16x16x32_f16 v[94:97], v[136:139], v[112:115], v[94:97]
	s_waitcnt lgkmcnt(8)
	v_mfma_f32_16x16x32_f16 v[2:5], v[156:159], v[140:143], v[2:5]
	s_waitcnt lgkmcnt(7)
	v_mfma_f32_16x16x32_f16 v[6:9], v[160:163], v[140:143], v[6:9]
	s_waitcnt lgkmcnt(6)
	v_mfma_f32_16x16x32_f16 v[10:13], v[164:167], v[140:143], v[10:13]
	s_waitcnt lgkmcnt(5)
	v_mfma_f32_16x16x32_f16 v[14:17], v[168:171], v[140:143], v[14:17]
	s_waitcnt lgkmcnt(4)
	v_mfma_f32_16x16x32_f16 v[18:21], v[172:175], v[140:143], v[18:21]
	s_waitcnt lgkmcnt(3)
	v_mfma_f32_16x16x32_f16 v[22:25], v[176:179], v[140:143], v[22:25]
	s_waitcnt lgkmcnt(2)
	v_mfma_f32_16x16x32_f16 v[26:29], v[156:159], v[144:147], v[26:29]
	v_mfma_f32_16x16x32_f16 v[30:33], v[160:163], v[144:147], v[30:33]
	v_mfma_f32_16x16x32_f16 v[34:37], v[164:167], v[144:147], v[34:37]
	v_mfma_f32_16x16x32_f16 v[38:41], v[168:171], v[144:147], v[38:41]
	v_mfma_f32_16x16x32_f16 v[42:45], v[172:175], v[144:147], v[42:45]
	v_mfma_f32_16x16x32_f16 v[46:49], v[176:179], v[144:147], v[46:49]
	s_waitcnt lgkmcnt(1)
	v_mfma_f32_16x16x32_f16 v[50:53], v[156:159], v[148:151], v[50:53]
	v_mfma_f32_16x16x32_f16 v[54:57], v[160:163], v[148:151], v[54:57]
	v_mfma_f32_16x16x32_f16 v[58:61], v[164:167], v[148:151], v[58:61]
	v_mfma_f32_16x16x32_f16 v[62:65], v[168:171], v[148:151], v[62:65]
	v_mfma_f32_16x16x32_f16 v[66:69], v[172:175], v[148:151], v[66:69]
	v_mfma_f32_16x16x32_f16 v[70:73], v[176:179], v[148:151], v[70:73]
	s_waitcnt lgkmcnt(0)
	v_mfma_f32_16x16x32_f16 v[74:77], v[156:159], v[152:155], v[74:77]
	v_mfma_f32_16x16x32_f16 v[78:81], v[160:163], v[152:155], v[78:81]
	v_mfma_f32_16x16x32_f16 v[82:85], v[164:167], v[152:155], v[82:85]
	v_mfma_f32_16x16x32_f16 v[86:89], v[168:171], v[152:155], v[86:89]
	v_mfma_f32_16x16x32_f16 v[90:93], v[172:175], v[152:155], v[90:93]
	v_mfma_f32_16x16x32_f16 v[94:97], v[176:179], v[152:155], v[94:97]
.LBB2_6:
	s_load_dwordx2 s[6:7], s[0:1], 0x20
	v_and_b32_e32 v164, 63, v0
	v_and_b32_e32 v165, 15, v164
	v_lshrrev_b32_e32 v166, 4, v164
	s_add_i32 s35, s15, s16
	s_add_i32 s28, s35, 0
	s_lshr_b32 s28, s28, 10
	s_add_i32 s29, s35, 16
	s_lshr_b32 s29, s29, 10
	s_add_i32 s30, s35, 32
	s_lshr_b32 s30, s30, 10
	s_add_i32 s31, s35, 48
	s_lshr_b32 s31, s31, 10
	s_add_i32 s32, s35, 64
	s_lshr_b32 s32, s32, 10
	s_add_i32 s33, s35, 80
	s_lshr_b32 s33, s33, 10
	s_mov_b32 s34, 0x3e38aa3b
	s_add_i32 s36, s19, s20
	s_and_b32 s37, s36, 2047
	s_lshl_b32 s37, s37, 8
	v_lshlrev_b32_e32 v167, 8, v165
	v_lshl_add_u32 v167, v166, 4, v167
	v_add_u32_e32 v167, s37, v167
	s_and_b32 s38, s16, 63
	s_lshl_b32 s38, s38, 2
	s_add_i32 s40, s38, 0
	s_and_b32 s40, s40, 255
	s_add_i32 s41, s38, 64
	s_and_b32 s41, s41, 255
	s_add_i32 s42, s38, 128
	s_and_b32 s42, s42, 255
	s_add_i32 s43, s38, 192
	s_and_b32 s43, s43, 255
	s_cmp_lt_u32 s28, 2
	s_cbranch_scc0 .Lq8_notab
	v_add_u32_e32 v168, s40, v167
	global_load_dwordx4 v[100:103], v168, s[12:13]
	v_add_u32_e32 v170, s41, v167
	global_load_dwordx4 v[104:107], v170, s[12:13]
	v_add_u32_e32 v168, s42, v167
	global_load_dwordx4 v[108:111], v168, s[12:13]
	v_add_u32_e32 v170, s43, v167
	global_load_dwordx4 v[112:115], v170, s[12:13]
	v_add_u32_e32 v168, s40, v167
	v_add_u32_e32 v168, 0x1000, v168
	global_load_dwordx4 v[116:119], v168, s[12:13]
	v_add_u32_e32 v170, s41, v167
	v_add_u32_e32 v170, 0x1000, v170
	global_load_dwordx4 v[120:123], v170, s[12:13]
	v_add_u32_e32 v168, s42, v167
	v_add_u32_e32 v168, 0x1000, v168
	global_load_dwordx4 v[124:127], v168, s[12:13]
	v_add_u32_e32 v170, s43, v167
	v_add_u32_e32 v170, 0x1000, v170
	global_load_dwordx4 v[128:131], v170, s[12:13]
	v_add_u32_e32 v168, s40, v167
	v_add_u32_e32 v168, 0x2000, v168
	global_load_dwordx4 v[132:135], v168, s[12:13]
	v_add_u32_e32 v170, s41, v167
	v_add_u32_e32 v170, 0x2000, v170
	global_load_dwordx4 v[136:139], v170, s[12:13]
	v_add_u32_e32 v168, s42, v167
	v_add_u32_e32 v168, 0x2000, v168
	global_load_dwordx4 v[140:143], v168, s[12:13]
	v_add_u32_e32 v170, s43, v167
	v_add_u32_e32 v170, 0x2000, v170
	global_load_dwordx4 v[144:147], v170, s[12:13]
	v_add_u32_e32 v168, s40, v167
	v_add_u32_e32 v168, 0x3000, v168
	global_load_dwordx4 v[148:151], v168, s[12:13]
	v_add_u32_e32 v170, s41, v167
	v_add_u32_e32 v170, 0x3000, v170
	global_load_dwordx4 v[152:155], v170, s[12:13]
	v_add_u32_e32 v168, s42, v167
	v_add_u32_e32 v168, 0x3000, v168
	global_load_dwordx4 v[156:159], v168, s[12:13]
	v_add_u32_e32 v170, s43, v167
	v_add_u32_e32 v170, 0x3000, v170
	global_load_dwordx4 v[160:163], v170, s[12:13]
.Lq8_notab:
	s_barrier
	s_mul_i32 s39, s14, 0x3400
	v_mul_u32_u24_e32 v169, 0xd0, v165
	v_lshl_add_u32 v169, v166, 3, v169
	v_add_u32_e32 v169, s39, v169
	v_add_u32_e32 v171, 0, v164
	v_mul_u32_u24_e32 v172, 0x1556, v171
	v_lshrrev_b32_e32 v172, 16, v172
	v_mul_u32_u24_e32 v173, 12, v172
	v_sub_u32_e32 v173, v171, v173
	v_mul_u32_u24_e32 v181, 0xd0, v172
	v_lshl_add_u32 v181, v173, 4, v181
	v_add_u32_e32 v181, s39, v181
	v_lshl_add_u32 v174, v173, 3, s35
	v_lshrrev_b32_e32 v175, 6, v174
	v_and_b32_e32 v174, 63, v174
	v_lshlrev_b32_e32 v175, 12, v175
	v_add3_u32 v175, v175, s36, v172
	v_lshlrev_b32_e32 v175, 7, v175
	v_lshl_add_u32 v184, v174, 1, v175
	v_add_u32_e32 v185, 0x1000, v184
	v_add_u32_e32 v171, 64, v164
	v_mul_u32_u24_e32 v172, 0x1556, v171
	v_lshrrev_b32_e32 v172, 16, v172
	v_mul_u32_u24_e32 v173, 12, v172
	v_sub_u32_e32 v173, v171, v173
	v_mul_u32_u24_e32 v182, 0xd0, v172
	v_lshl_add_u32 v182, v173, 4, v182
	v_add_u32_e32 v182, s39, v182
	v_lshl_add_u32 v174, v173, 3, s35
	v_lshrrev_b32_e32 v175, 6, v174
	v_and_b32_e32 v174, 63, v174
	v_lshlrev_b32_e32 v175, 12, v175
	v_add3_u32 v175, v175, s36, v172
	v_lshlrev_b32_e32 v175, 7, v175
	v_lshl_add_u32 v186, v174, 1, v175
	v_add_u32_e32 v187, 0x1000, v186
	v_add_u32_e32 v171, 128, v164
	v_mul_u32_u24_e32 v172, 0x1556, v171
	v_lshrrev_b32_e32 v172, 16, v172
	v_mul_u32_u24_e32 v173, 12, v172
	v_sub_u32_e32 v173, v171, v173
	v_mul_u32_u24_e32 v183, 0xd0, v172
	v_lshl_add_u32 v183, v173, 4, v183
	v_add_u32_e32 v183, s39, v183
	v_lshl_add_u32 v174, v173, 3, s35
	v_lshrrev_b32_e32 v175, 6, v174
	v_and_b32_e32 v174, 63, v174
	v_lshlrev_b32_e32 v175, 12, v175
	v_add3_u32 v175, v175, s36, v172
	v_lshlrev_b32_e32 v175, 7, v175
	v_lshl_add_u32 v188, v174, 1, v175
	v_add_u32_e32 v189, 0x1000, v188
	s_waitcnt lgkmcnt(0)
	s_waitcnt vmcnt(12)
	s_cmp_lt_u32 s28, 2
	s_cbranch_scc0 .Lq8_nr_0_0
	v_mul_f32_e32 v176, v3, v101
	v_mul_f32_e32 v177, v2, v101
	v_fma_f32 v2, v2, v100, -v176
	v_fma_f32 v3, v3, v100, v177
	v_mul_f32_e32 v176, v5, v103
	v_mul_f32_e32 v177, v4, v103
	v_fma_f32 v4, v4, v102, -v176
	v_fma_f32 v5, v5, v102, v177
	s_cmp_eq_u32 s28, 0
	s_cbranch_scc0 .Lq8_nr_0_0
	v_mul_f32_e32 v2, s34, v2
	v_mul_f32_e32 v3, s34, v3
	v_mul_f32_e32 v4, s34, v4
	v_mul_f32_e32 v5, s34, v5
.Lq8_nr_0_0:
	v_cvt_pk_f16_f32 v178, v2, v3
	v_cvt_pk_f16_f32 v179, v4, v5
	ds_write_b64 v169, v[178:179] offset:0
	s_cmp_lt_u32 s29, 2
	s_cbranch_scc0 .Lq8_nr_0_1
	v_mul_f32_e32 v176, v7, v105
	v_mul_f32_e32 v177, v6, v105
	v_fma_f32 v6, v6, v104, -v176
	v_fma_f32 v7, v7, v104, v177
	v_mul_f32_e32 v176, v9, v107
	v_mul_f32_e32 v177, v8, v107
	v_fma_f32 v8, v8, v106, -v176
	v_fma_f32 v9, v9, v106, v177
	s_cmp_eq_u32 s29, 0
	s_cbranch_scc0 .Lq8_nr_0_1
	v_mul_f32_e32 v6, s34, v6
	v_mul_f32_e32 v7, s34, v7
	v_mul_f32_e32 v8, s34, v8
	v_mul_f32_e32 v9, s34, v9
.Lq8_nr_0_1:
	v_cvt_pk_f16_f32 v196, v6, v7
	v_cvt_pk_f16_f32 v197, v8, v9
	ds_write_b64 v169, v[196:197] offset:32
	s_cmp_lt_u32 s30, 2
	s_cbranch_scc0 .Lq8_nr_0_2
	v_mul_f32_e32 v176, v11, v109
	v_mul_f32_e32 v177, v10, v109
	v_fma_f32 v10, v10, v108, -v176
	v_fma_f32 v11, v11, v108, v177
	v_mul_f32_e32 v176, v13, v111
	v_mul_f32_e32 v177, v12, v111
	v_fma_f32 v12, v12, v110, -v176
	v_fma_f32 v13, v13, v110, v177
	s_cmp_eq_u32 s30, 0
	s_cbranch_scc0 .Lq8_nr_0_2
	v_mul_f32_e32 v10, s34, v10
	v_mul_f32_e32 v11, s34, v11
	v_mul_f32_e32 v12, s34, v12
	v_mul_f32_e32 v13, s34, v13
.Lq8_nr_0_2:
	v_cvt_pk_f16_f32 v178, v10, v11
	v_cvt_pk_f16_f32 v179, v12, v13
	ds_write_b64 v169, v[178:179] offset:64
	s_cmp_lt_u32 s31, 2
	s_cbranch_scc0 .Lq8_nr_0_3
	v_mul_f32_e32 v176, v15, v113
	v_mul_f32_e32 v177, v14, v113
	v_fma_f32 v14, v14, v112, -v176
	v_fma_f32 v15, v15, v112, v177
	v_mul_f32_e32 v176, v17, v115
	v_mul_f32_e32 v177, v16, v115
	v_fma_f32 v16, v16, v114, -v176
	v_fma_f32 v17, v17, v114, v177
	s_cmp_eq_u32 s31, 0
	s_cbranch_scc0 .Lq8_nr_0_3
	v_mul_f32_e32 v14, s34, v14
	v_mul_f32_e32 v15, s34, v15
	v_mul_f32_e32 v16, s34, v16
	v_mul_f32_e32 v17, s34, v17
.Lq8_nr_0_3:
	v_cvt_pk_f16_f32 v196, v14, v15
	v_cvt_pk_f16_f32 v197, v16, v17
	ds_write_b64 v169, v[196:197] offset:96
	s_cmp_lt_u32 s32, 2
	s_cbranch_scc0 .Lq8_nr_0_4
	v_mul_f32_e32 v176, v19, v101
	v_mul_f32_e32 v177, v18, v101
	v_fma_f32 v18, v18, v100, -v176
	v_fma_f32 v19, v19, v100, v177
	v_mul_f32_e32 v176, v21, v103
	v_mul_f32_e32 v177, v20, v103
	v_fma_f32 v20, v20, v102, -v176
	v_fma_f32 v21, v21, v102, v177
	s_cmp_eq_u32 s32, 0
	s_cbranch_scc0 .Lq8_nr_0_4
	v_mul_f32_e32 v18, s34, v18
	v_mul_f32_e32 v19, s34, v19
	v_mul_f32_e32 v20, s34, v20
	v_mul_f32_e32 v21, s34, v21
.Lq8_nr_0_4:
	v_cvt_pk_f16_f32 v178, v18, v19
	v_cvt_pk_f16_f32 v179, v20, v21
	ds_write_b64 v169, v[178:179] offset:128
	s_cmp_lt_u32 s33, 2
	s_cbranch_scc0 .Lq8_nr_0_5
	v_mul_f32_e32 v176, v23, v105
	v_mul_f32_e32 v177, v22, v105
	v_fma_f32 v22, v22, v104, -v176
	v_fma_f32 v23, v23, v104, v177
	v_mul_f32_e32 v176, v25, v107
	v_mul_f32_e32 v177, v24, v107
	v_fma_f32 v24, v24, v106, -v176
	v_fma_f32 v25, v25, v106, v177
	s_cmp_eq_u32 s33, 0
	s_cbranch_scc0 .Lq8_nr_0_5
	v_mul_f32_e32 v22, s34, v22
	v_mul_f32_e32 v23, s34, v23
	v_mul_f32_e32 v24, s34, v24
	v_mul_f32_e32 v25, s34, v25
.Lq8_nr_0_5:
	v_cvt_pk_f16_f32 v196, v22, v23
	v_cvt_pk_f16_f32 v197, v24, v25
	ds_write_b64 v169, v[196:197] offset:160
	s_waitcnt lgkmcnt(0)
	ds_read_b128 v[200:203], v181 offset:0
	ds_read_b128 v[204:207], v182 offset:0
	ds_read_b128 v[208:211], v183 offset:0
	s_waitcnt lgkmcnt(2)
	global_store_dwordx4 v184, v[200:203], s[6:7] sc1
	s_waitcnt lgkmcnt(1)
	global_store_dwordx4 v186, v[204:207], s[6:7] sc1
	s_waitcnt lgkmcnt(0)
	global_store_dwordx4 v188, v[208:211], s[6:7] sc1
	s_waitcnt vmcnt(11)
	s_cmp_lt_u32 s28, 2
	s_cbranch_scc0 .Lq8_nr_1_0
	v_mul_f32_e32 v176, v27, v117
	v_mul_f32_e32 v177, v26, v117
	v_fma_f32 v26, v26, v116, -v176
	v_fma_f32 v27, v27, v116, v177
	v_mul_f32_e32 v176, v29, v119
	v_mul_f32_e32 v177, v28, v119
	v_fma_f32 v28, v28, v118, -v176
	v_fma_f32 v29, v29, v118, v177
	s_cmp_eq_u32 s28, 0
	s_cbranch_scc0 .Lq8_nr_1_0
	v_mul_f32_e32 v26, s34, v26
	v_mul_f32_e32 v27, s34, v27
	v_mul_f32_e32 v28, s34, v28
	v_mul_f32_e32 v29, s34, v29
.Lq8_nr_1_0:
	v_cvt_pk_f16_f32 v178, v26, v27
	v_cvt_pk_f16_f32 v179, v28, v29
	ds_write_b64 v169, v[178:179] offset:3328
	s_cmp_lt_u32 s29, 2
	s_cbranch_scc0 .Lq8_nr_1_1
	v_mul_f32_e32 v176, v31, v121
	v_mul_f32_e32 v177, v30, v121
	v_fma_f32 v30, v30, v120, -v176
	v_fma_f32 v31, v31, v120, v177
	v_mul_f32_e32 v176, v33, v123
	v_mul_f32_e32 v177, v32, v123
	v_fma_f32 v32, v32, v122, -v176
	v_fma_f32 v33, v33, v122, v177
	s_cmp_eq_u32 s29, 0
	s_cbranch_scc0 .Lq8_nr_1_1
	v_mul_f32_e32 v30, s34, v30
	v_mul_f32_e32 v31, s34, v31
	v_mul_f32_e32 v32, s34, v32
	v_mul_f32_e32 v33, s34, v33
.Lq8_nr_1_1:
	v_cvt_pk_f16_f32 v196, v30, v31
	v_cvt_pk_f16_f32 v197, v32, v33
	ds_write_b64 v169, v[196:197] offset:3360
	s_cmp_lt_u32 s30, 2
	s_cbranch_scc0 .Lq8_nr_1_2
	v_mul_f32_e32 v176, v35, v125
	v_mul_f32_e32 v177, v34, v125
	v_fma_f32 v34, v34, v124, -v176
	v_fma_f32 v35, v35, v124, v177
	v_mul_f32_e32 v176, v37, v127
	v_mul_f32_e32 v177, v36, v127
	v_fma_f32 v36, v36, v126, -v176
	v_fma_f32 v37, v37, v126, v177
	s_cmp_eq_u32 s30, 0
	s_cbranch_scc0 .Lq8_nr_1_2
	v_mul_f32_e32 v34, s34, v34
	v_mul_f32_e32 v35, s34, v35
	v_mul_f32_e32 v36, s34, v36
	v_mul_f32_e32 v37, s34, v37
.Lq8_nr_1_2:
	v_cvt_pk_f16_f32 v178, v34, v35
	v_cvt_pk_f16_f32 v179, v36, v37
	ds_write_b64 v169, v[178:179] offset:3392
	s_cmp_lt_u32 s31, 2
	s_cbranch_scc0 .Lq8_nr_1_3
	v_mul_f32_e32 v176, v39, v129
	v_mul_f32_e32 v177, v38, v129
	v_fma_f32 v38, v38, v128, -v176
	v_fma_f32 v39, v39, v128, v177
	v_mul_f32_e32 v176, v41, v131
	v_mul_f32_e32 v177, v40, v131
	v_fma_f32 v40, v40, v130, -v176
	v_fma_f32 v41, v41, v130, v177
	s_cmp_eq_u32 s31, 0
	s_cbranch_scc0 .Lq8_nr_1_3
	v_mul_f32_e32 v38, s34, v38
	v_mul_f32_e32 v39, s34, v39
	v_mul_f32_e32 v40, s34, v40
	v_mul_f32_e32 v41, s34, v41
.Lq8_nr_1_3:
	v_cvt_pk_f16_f32 v196, v38, v39
	v_cvt_pk_f16_f32 v197, v40, v41
	ds_write_b64 v169, v[196:197] offset:3424
	s_cmp_lt_u32 s32, 2
	s_cbranch_scc0 .Lq8_nr_1_4
	v_mul_f32_e32 v176, v43, v117
	v_mul_f32_e32 v177, v42, v117
	v_fma_f32 v42, v42, v116, -v176
	v_fma_f32 v43, v43, v116, v177
	v_mul_f32_e32 v176, v45, v119
	v_mul_f32_e32 v177, v44, v119
	v_fma_f32 v44, v44, v118, -v176
	v_fma_f32 v45, v45, v118, v177
	s_cmp_eq_u32 s32, 0
	s_cbranch_scc0 .Lq8_nr_1_4
	v_mul_f32_e32 v42, s34, v42
	v_mul_f32_e32 v43, s34, v43
	v_mul_f32_e32 v44, s34, v44
	v_mul_f32_e32 v45, s34, v45
.Lq8_nr_1_4:
	v_cvt_pk_f16_f32 v178, v42, v43
	v_cvt_pk_f16_f32 v179, v44, v45
	ds_write_b64 v169, v[178:179] offset:3456
	s_cmp_lt_u32 s33, 2
	s_cbranch_scc0 .Lq8_nr_1_5
	v_mul_f32_e32 v176, v47, v121
	v_mul_f32_e32 v177, v46, v121
	v_fma_f32 v46, v46, v120, -v176
	v_fma_f32 v47, v47, v120, v177
	v_mul_f32_e32 v176, v49, v123
	v_mul_f32_e32 v177, v48, v123
	v_fma_f32 v48, v48, v122, -v176
	v_fma_f32 v49, v49, v122, v177
	s_cmp_eq_u32 s33, 0
	s_cbranch_scc0 .Lq8_nr_1_5
	v_mul_f32_e32 v46, s34, v46
	v_mul_f32_e32 v47, s34, v47
	v_mul_f32_e32 v48, s34, v48
	v_mul_f32_e32 v49, s34, v49
.Lq8_nr_1_5:
	v_cvt_pk_f16_f32 v196, v46, v47
	v_cvt_pk_f16_f32 v197, v48, v49
	ds_write_b64 v169, v[196:197] offset:3488
	s_waitcnt lgkmcnt(0)
	ds_read_b128 v[200:203], v181 offset:3328
	ds_read_b128 v[204:207], v182 offset:3328
	ds_read_b128 v[208:211], v183 offset:3328
	s_waitcnt lgkmcnt(2)
	global_store_dwordx4 v184, v[200:203], s[6:7] offset:2048 sc1
	s_waitcnt lgkmcnt(1)
	global_store_dwordx4 v186, v[204:207], s[6:7] offset:2048 sc1
	s_waitcnt lgkmcnt(0)
	global_store_dwordx4 v188, v[208:211], s[6:7] offset:2048 sc1
	s_waitcnt vmcnt(10)
	s_cmp_lt_u32 s28, 2
	s_cbranch_scc0 .Lq8_nr_2_0
	v_mul_f32_e32 v176, v51, v133
	v_mul_f32_e32 v177, v50, v133
	v_fma_f32 v50, v50, v132, -v176
	v_fma_f32 v51, v51, v132, v177
	v_mul_f32_e32 v176, v53, v135
	v_mul_f32_e32 v177, v52, v135
	v_fma_f32 v52, v52, v134, -v176
	v_fma_f32 v53, v53, v134, v177
	s_cmp_eq_u32 s28, 0
	s_cbranch_scc0 .Lq8_nr_2_0
	v_mul_f32_e32 v50, s34, v50
	v_mul_f32_e32 v51, s34, v51
	v_mul_f32_e32 v52, s34, v52
	v_mul_f32_e32 v53, s34, v53
.Lq8_nr_2_0:
	v_cvt_pk_f16_f32 v178, v50, v51
	v_cvt_pk_f16_f32 v179, v52, v53
	ds_write_b64 v169, v[178:179] offset:6656
	s_cmp_lt_u32 s29, 2
	s_cbranch_scc0 .Lq8_nr_2_1
	v_mul_f32_e32 v176, v55, v137
	v_mul_f32_e32 v177, v54, v137
	v_fma_f32 v54, v54, v136, -v176
	v_fma_f32 v55, v55, v136, v177
	v_mul_f32_e32 v176, v57, v139
	v_mul_f32_e32 v177, v56, v139
	v_fma_f32 v56, v56, v138, -v176
	v_fma_f32 v57, v57, v138, v177
	s_cmp_eq_u32 s29, 0
	s_cbranch_scc0 .Lq8_nr_2_1
	v_mul_f32_e32 v54, s34, v54
	v_mul_f32_e32 v55, s34, v55
	v_mul_f32_e32 v56, s34, v56
	v_mul_f32_e32 v57, s34, v57
.Lq8_nr_2_1:
	v_cvt_pk_f16_f32 v196, v54, v55
	v_cvt_pk_f16_f32 v197, v56, v57
	ds_write_b64 v169, v[196:197] offset:6688
	s_cmp_lt_u32 s30, 2
	s_cbranch_scc0 .Lq8_nr_2_2
	v_mul_f32_e32 v176, v59, v141
	v_mul_f32_e32 v177, v58, v141
	v_fma_f32 v58, v58, v140, -v176
	v_fma_f32 v59, v59, v140, v177
	v_mul_f32_e32 v176, v61, v143
	v_mul_f32_e32 v177, v60, v143
	v_fma_f32 v60, v60, v142, -v176
	v_fma_f32 v61, v61, v142, v177
	s_cmp_eq_u32 s30, 0
	s_cbranch_scc0 .Lq8_nr_2_2
	v_mul_f32_e32 v58, s34, v58
	v_mul_f32_e32 v59, s34, v59
	v_mul_f32_e32 v60, s34, v60
	v_mul_f32_e32 v61, s34, v61
.Lq8_nr_2_2:
	v_cvt_pk_f16_f32 v178, v58, v59
	v_cvt_pk_f16_f32 v179, v60, v61
	ds_write_b64 v169, v[178:179] offset:6720
	s_cmp_lt_u32 s31, 2
	s_cbranch_scc0 .Lq8_nr_2_3
	v_mul_f32_e32 v176, v63, v145
	v_mul_f32_e32 v177, v62, v145
	v_fma_f32 v62, v62, v144, -v176
	v_fma_f32 v63, v63, v144, v177
	v_mul_f32_e32 v176, v65, v147
	v_mul_f32_e32 v177, v64, v147
	v_fma_f32 v64, v64, v146, -v176
	v_fma_f32 v65, v65, v146, v177
	s_cmp_eq_u32 s31, 0
	s_cbranch_scc0 .Lq8_nr_2_3
	v_mul_f32_e32 v62, s34, v62
	v_mul_f32_e32 v63, s34, v63
	v_mul_f32_e32 v64, s34, v64
	v_mul_f32_e32 v65, s34, v65
.Lq8_nr_2_3:
	v_cvt_pk_f16_f32 v196, v62, v63
	v_cvt_pk_f16_f32 v197, v64, v65
	ds_write_b64 v169, v[196:197] offset:6752
	s_cmp_lt_u32 s32, 2
	s_cbranch_scc0 .Lq8_nr_2_4
	v_mul_f32_e32 v176, v67, v133
	v_mul_f32_e32 v177, v66, v133
	v_fma_f32 v66, v66, v132, -v176
	v_fma_f32 v67, v67, v132, v177
	v_mul_f32_e32 v176, v69, v135
	v_mul_f32_e32 v177, v68, v135
	v_fma_f32 v68, v68, v134, -v176
	v_fma_f32 v69, v69, v134, v177
	s_cmp_eq_u32 s32, 0
	s_cbranch_scc0 .Lq8_nr_2_4
	v_mul_f32_e32 v66, s34, v66
	v_mul_f32_e32 v67, s34, v67
	v_mul_f32_e32 v68, s34, v68
	v_mul_f32_e32 v69, s34, v69
.Lq8_nr_2_4:
	v_cvt_pk_f16_f32 v178, v66, v67
	v_cvt_pk_f16_f32 v179, v68, v69
	ds_write_b64 v169, v[178:179] offset:6784
	s_cmp_lt_u32 s33, 2
	s_cbranch_scc0 .Lq8_nr_2_5
	v_mul_f32_e32 v176, v71, v137
	v_mul_f32_e32 v177, v70, v137
	v_fma_f32 v70, v70, v136, -v176
	v_fma_f32 v71, v71, v136, v177
	v_mul_f32_e32 v176, v73, v139
	v_mul_f32_e32 v177, v72, v139
	v_fma_f32 v72, v72, v138, -v176
	v_fma_f32 v73, v73, v138, v177
	s_cmp_eq_u32 s33, 0
	s_cbranch_scc0 .Lq8_nr_2_5
	v_mul_f32_e32 v70, s34, v70
	v_mul_f32_e32 v71, s34, v71
	v_mul_f32_e32 v72, s34, v72
	v_mul_f32_e32 v73, s34, v73
.Lq8_nr_2_5:
	v_cvt_pk_f16_f32 v196, v70, v71
	v_cvt_pk_f16_f32 v197, v72, v73
	ds_write_b64 v169, v[196:197] offset:6816
	s_waitcnt lgkmcnt(0)
	ds_read_b128 v[200:203], v181 offset:6656
	ds_read_b128 v[204:207], v182 offset:6656
	ds_read_b128 v[208:211], v183 offset:6656
	s_waitcnt lgkmcnt(2)
	global_store_dwordx4 v185, v[200:203], s[6:7] sc1
	s_waitcnt lgkmcnt(1)
	global_store_dwordx4 v187, v[204:207], s[6:7] sc1
	s_waitcnt lgkmcnt(0)
	global_store_dwordx4 v189, v[208:211], s[6:7] sc1
	s_waitcnt vmcnt(9)
	s_cmp_lt_u32 s28, 2
	s_cbranch_scc0 .Lq8_nr_3_0
	v_mul_f32_e32 v176, v75, v149
	v_mul_f32_e32 v177, v74, v149
	v_fma_f32 v74, v74, v148, -v176
	v_fma_f32 v75, v75, v148, v177
	v_mul_f32_e32 v176, v77, v151
	v_mul_f32_e32 v177, v76, v151
	v_fma_f32 v76, v76, v150, -v176
	v_fma_f32 v77, v77, v150, v177
	s_cmp_eq_u32 s28, 0
	s_cbranch_scc0 .Lq8_nr_3_0
	v_mul_f32_e32 v74, s34, v74
	v_mul_f32_e32 v75, s34, v75
	v_mul_f32_e32 v76, s34, v76
	v_mul_f32_e32 v77, s34, v77
.Lq8_nr_3_0:
	v_cvt_pk_f16_f32 v178, v74, v75
	v_cvt_pk_f16_f32 v179, v76, v77
	ds_write_b64 v169, v[178:179] offset:9984
	s_cmp_lt_u32 s29, 2
	s_cbranch_scc0 .Lq8_nr_3_1
	v_mul_f32_e32 v176, v79, v153
	v_mul_f32_e32 v177, v78, v153
	v_fma_f32 v78, v78, v152, -v176
	v_fma_f32 v79, v79, v152, v177
	v_mul_f32_e32 v176, v81, v155
	v_mul_f32_e32 v177, v80, v155
	v_fma_f32 v80, v80, v154, -v176
	v_fma_f32 v81, v81, v154, v177
	s_cmp_eq_u32 s29, 0
	s_cbranch_scc0 .Lq8_nr_3_1
	v_mul_f32_e32 v78, s34, v78
	v_mul_f32_e32 v79, s34, v79
	v_mul_f32_e32 v80, s34, v80
	v_mul_f32_e32 v81, s34, v81
.Lq8_nr_3_1:
	v_cvt_pk_f16_f32 v196, v78, v79
	v_cvt_pk_f16_f32 v197, v80, v81
	ds_write_b64 v169, v[196:197] offset:10016
	s_cmp_lt_u32 s30, 2
	s_cbranch_scc0 .Lq8_nr_3_2
	v_mul_f32_e32 v176, v83, v157
	v_mul_f32_e32 v177, v82, v157
	v_fma_f32 v82, v82, v156, -v176
	v_fma_f32 v83, v83, v156, v177
	v_mul_f32_e32 v176, v85, v159
	v_mul_f32_e32 v177, v84, v159
	v_fma_f32 v84, v84, v158, -v176
	v_fma_f32 v85, v85, v158, v177
	s_cmp_eq_u32 s30, 0
	s_cbranch_scc0 .Lq8_nr_3_2
	v_mul_f32_e32 v82, s34, v82
	v_mul_f32_e32 v83, s34, v83
	v_mul_f32_e32 v84, s34, v84
	v_mul_f32_e32 v85, s34, v85
.Lq8_nr_3_2:
	v_cvt_pk_f16_f32 v178, v82, v83
	v_cvt_pk_f16_f32 v179, v84, v85
	ds_write_b64 v169, v[178:179] offset:10048
	s_cmp_lt_u32 s31, 2
	s_cbranch_scc0 .Lq8_nr_3_3
	v_mul_f32_e32 v176, v87, v161
	v_mul_f32_e32 v177, v86, v161
	v_fma_f32 v86, v86, v160, -v176
	v_fma_f32 v87, v87, v160, v177
	v_mul_f32_e32 v176, v89, v163
	v_mul_f32_e32 v177, v88, v163
	v_fma_f32 v88, v88, v162, -v176
	v_fma_f32 v89, v89, v162, v177
	s_cmp_eq_u32 s31, 0
	s_cbranch_scc0 .Lq8_nr_3_3
	v_mul_f32_e32 v86, s34, v86
	v_mul_f32_e32 v87, s34, v87
	v_mul_f32_e32 v88, s34, v88
	v_mul_f32_e32 v89, s34, v89
.Lq8_nr_3_3:
	v_cvt_pk_f16_f32 v196, v86, v87
	v_cvt_pk_f16_f32 v197, v88, v89
	ds_write_b64 v169, v[196:197] offset:10080
	s_cmp_lt_u32 s32, 2
	s_cbranch_scc0 .Lq8_nr_3_4
	v_mul_f32_e32 v176, v91, v149
	v_mul_f32_e32 v177, v90, v149
	v_fma_f32 v90, v90, v148, -v176
	v_fma_f32 v91, v91, v148, v177
	v_mul_f32_e32 v176, v93, v151
	v_mul_f32_e32 v177, v92, v151
	v_fma_f32 v92, v92, v150, -v176
	v_fma_f32 v93, v93, v150, v177
	s_cmp_eq_u32 s32, 0
	s_cbranch_scc0 .Lq8_nr_3_4
	v_mul_f32_e32 v90, s34, v90
	v_mul_f32_e32 v91, s34, v91
	v_mul_f32_e32 v92, s34, v92
	v_mul_f32_e32 v93, s34, v93
.Lq8_nr_3_4:
	v_cvt_pk_f16_f32 v178, v90, v91
	v_cvt_pk_f16_f32 v179, v92, v93
	ds_write_b64 v169, v[178:179] offset:10112
	s_cmp_lt_u32 s33, 2
	s_cbranch_scc0 .Lq8_nr_3_5
	v_mul_f32_e32 v176, v95, v153
	v_mul_f32_e32 v177, v94, v153
	v_fma_f32 v94, v94, v152, -v176
	v_fma_f32 v95, v95, v152, v177
	v_mul_f32_e32 v176, v97, v155
	v_mul_f32_e32 v177, v96, v155
	v_fma_f32 v96, v96, v154, -v176
	v_fma_f32 v97, v97, v154, v177
	s_cmp_eq_u32 s33, 0
	s_cbranch_scc0 .Lq8_nr_3_5
	v_mul_f32_e32 v94, s34, v94
	v_mul_f32_e32 v95, s34, v95
	v_mul_f32_e32 v96, s34, v96
	v_mul_f32_e32 v97, s34, v97
.Lq8_nr_3_5:
	v_cvt_pk_f16_f32 v196, v94, v95
	v_cvt_pk_f16_f32 v197, v96, v97
	ds_write_b64 v169, v[196:197] offset:10144
	s_waitcnt lgkmcnt(0)
	ds_read_b128 v[200:203], v181 offset:9984
	ds_read_b128 v[204:207], v182 offset:9984
	ds_read_b128 v[208:211], v183 offset:9984
	s_waitcnt lgkmcnt(2)
	global_store_dwordx4 v185, v[200:203], s[6:7] offset:2048 sc1
	s_waitcnt lgkmcnt(1)
	global_store_dwordx4 v187, v[204:207], s[6:7] offset:2048 sc1
	s_waitcnt lgkmcnt(0)
	global_store_dwordx4 v189, v[208:211], s[6:7] offset:2048 sc1
	s_endpgm
	.p2align	8

	.amdhsa_kernel _Z11gemm_kernelILi256ELi192ELi4ELi2ELi4ELi2ELi2ELi0EEvPKDF16_S1_iiiPDF16_PfPK15HIP_vector_typeIfLj2EE
		.amdhsa_group_segment_fixed_size 0
		.amdhsa_private_segment_fixed_size 0
		.amdhsa_kernarg_size 56
		.amdhsa_user_sgpr_count 2
		.amdhsa_user_sgpr_dispatch_ptr 0
		.amdhsa_user_sgpr_queue_ptr 0
		.amdhsa_user_sgpr_kernarg_segment_ptr 1
		.amdhsa_user_sgpr_dispatch_id 0
		.amdhsa_user_sgpr_kernarg_preload_length 0
		.amdhsa_user_sgpr_kernarg_preload_offset 0
		.amdhsa_user_sgpr_private_segment_size 0
		.amdhsa_uses_dynamic_stack 0
		.amdhsa_enable_private_segment 0
		.amdhsa_system_sgpr_workgroup_id_x 1
		.amdhsa_system_sgpr_workgroup_id_y 0
		.amdhsa_system_sgpr_workgroup_id_z 0
		.amdhsa_system_sgpr_workgroup_info 0
		.amdhsa_system_vgpr_workitem_id 0
		.amdhsa_next_free_vgpr 212
		.amdhsa_next_free_sgpr 44
		.amdhsa_accum_offset 212
		.amdhsa_reserve_vcc 1
		.amdhsa_float_round_mode_32 0
		.amdhsa_float_round_mode_16_64 0
		.amdhsa_float_denorm_mode_32 3
		.amdhsa_float_denorm_mode_16_64 3
		.amdhsa_dx10_clamp 1
		.amdhsa_ieee_mode 1
		.amdhsa_fp16_overflow 0
		.amdhsa_tg_split 0
		.amdhsa_exception_fp_ieee_invalid_op 0
		.amdhsa_exception_fp_denorm_src 0
		.amdhsa_exception_fp_ieee_div_zero 0
		.amdhsa_exception_fp_ieee_overflow 0
		.amdhsa_exception_fp_ieee_underflow 0
		.amdhsa_exception_fp_ieee_inexact 0
		.amdhsa_exception_int_div_zero 0
	.end_amdhsa_kernel

amdhsa.kernels:
  - .agpr_count:     0
    .args:
      - .actual_access:  read_only
        .address_space:  global
        .offset:         0
        .size:           8
        .value_kind:     global_buffer
      - .actual_access:  read_only
        .address_space:  global
        .offset:         8
        .size:           8
        .value_kind:     global_buffer
      - .actual_access:  read_only
        .address_space:  global
        .offset:         16
        .size:           8
        .value_kind:     global_buffer
      - .actual_access:  read_only
        .address_space:  global
        .offset:         24
        .size:           8
        .value_kind:     global_buffer
      - .actual_access:  read_only
        .address_space:  global
        .offset:         32
        .size:           8
        .value_kind:     global_buffer
      - .actual_access:  read_only
        .address_space:  global
        .offset:         40
        .size:           8
        .value_kind:     global_buffer
      - .actual_access:  write_only
        .address_space:  global
        .offset:         48
        .size:           8
        .value_kind:     global_buffer
      - .actual_access:  write_only
        .address_space:  global
        .offset:         56
        .size:           8
        .value_kind:     global_buffer
      - .actual_access:  read_only
        .address_space:  global
        .offset:         64
        .size:           8
        .value_kind:     global_buffer
      - .actual_access:  write_only
        .address_space:  global
        .offset:         72
        .size:           8
        .value_kind:     global_buffer
      - .actual_access:  write_only
        .address_space:  global
        .offset:         80
        .size:           8
        .value_kind:     global_buffer
      - .offset:         88
        .size:           128
        .value_kind:     by_value
    .group_segment_fixed_size: 0
    .kernarg_segment_align: 8
    .kernarg_segment_size: 216
    .language:       OpenCL C
    .language_version:
      - 2
      - 0
    .max_flat_workgroup_size: 256
    .name:           _Z11prep_kernelPKfS0_S0_S0_S0_PKiPDF16_S3_S3_P15HIP_vector_typeIfLj2EEPi5Freqs
    .private_segment_fixed_size: 0
    .sgpr_count:     22
    .sgpr_spill_count: 0
    .symbol:         _Z11prep_kernelPKfS0_S0_S0_S0_PKiPDF16_S3_S3_P15HIP_vector_typeIfLj2EEPi5Freqs.kd
    .uniform_work_group_size: 1
    .uses_dynamic_stack: false
    .vgpr_count:     32
    .vgpr_spill_count: 0
    .wavefront_size: 64
  - .agpr_count:     0
    .args:
      - .address_space:  global
        .offset:         0
        .size:           8
        .value_kind:     global_buffer
      - .address_space:  global
        .offset:         8
        .size:           8
        .value_kind:     global_buffer
      - .address_space:  global
        .offset:         16
        .size:           8
        .value_kind:     global_buffer
      - .address_space:  global
        .offset:         24
        .size:           8
        .value_kind:     global_buffer
      - .address_space:  global
        .offset:         32
        .size:           8
        .value_kind:     global_buffer
      - .address_space:  global
        .offset:         40
        .size:           8
        .value_kind:     global_buffer
      - .address_space:  global
        .offset:         48
        .size:           8
        .value_kind:     global_buffer
      - .actual_access:  read_only
        .address_space:  global
        .offset:         56
        .size:           8
        .value_kind:     global_buffer
      - .actual_access:  write_only
        .address_space:  global
        .offset:         64
        .size:           8
        .value_kind:     global_buffer
    .group_segment_fixed_size: 0
    .kernarg_segment_align: 8
    .kernarg_segment_size: 72
    .language:       OpenCL C
    .language_version:
      - 2
      - 0
    .max_flat_workgroup_size: 256
    .name:           _ZN3att10attn64_fwdEPKDF16_S1_S1_PDF16_S2_P15HIP_vector_typeIfLj2EEPiPKfS2_
    .private_segment_fixed_size: 0
    .sgpr_count:     78
    .sgpr_spill_count: 0
    .symbol:         _ZN3att10attn64_fwdEPKDF16_S1_S1_PDF16_S2_P15HIP_vector_typeIfLj2EEPiPKfS2_.kd
    .uniform_work_group_size: 1
    .uses_dynamic_stack: false
    .vgpr_count:     240
    .vgpr_spill_count: 0
    .wavefront_size: 64
  - .agpr_count:     0
    .args:
      - .address_space:  global
        .offset:         0
        .size:           8
        .value_kind:     global_buffer
      - .address_space:  global
        .offset:         8
        .size:           8
        .value_kind:     global_buffer
      - .offset:         16
        .size:           4
        .value_kind:     by_value
      - .offset:         20
        .size:           4
        .value_kind:     by_value
      - .offset:         24
        .size:           4
        .value_kind:     by_value
      - .actual_access:  write_only
        .address_space:  global
        .offset:         32
        .size:           8
        .value_kind:     global_buffer
      - .actual_access:  read_only
        .address_space:  global
        .offset:         40
        .size:           8
        .value_kind:     global_buffer
      - .actual_access:  read_only
        .address_space:  global
        .offset:         48
        .size:           8
        .value_kind:     global_buffer
    .group_segment_fixed_size: 0
    .kernarg_segment_align: 8
    .kernarg_segment_size: 56
    .language:       OpenCL C
    .language_version:
      - 2
      - 0
    .max_flat_workgroup_size: 512
    .name:           _Z11gemm_kernelILi256ELi192ELi4ELi2ELi4ELi2ELi2ELi0EEvPKDF16_S1_iiiPDF16_PfPK15HIP_vector_typeIfLj2EE
    .private_segment_fixed_size: 0
    .sgpr_count:     50
    .sgpr_spill_count: 0
    .symbol:         _Z11gemm_kernelILi256ELi192ELi4ELi2ELi4ELi2ELi2ELi0EEvPKDF16_S1_iiiPDF16_PfPK15HIP_vector_typeIfLj2EE.kd
    .uniform_work_group_size: 1
    .uses_dynamic_stack: false
    .vgpr_count:     212
    .vgpr_spill_count: 0
    .wavefront_size: 64
  - .agpr_count:     0
    .args:
      - .address_space:  global
        .offset:         0
        .size:           8
        .value_kind:     global_buffer
      - .address_space:  global
        .offset:         8
        .size:           8
        .value_kind:     global_buffer
      - .offset:         16
        .size:           4
        .value_kind:     by_value
      - .offset:         20
        .size:           4
        .value_kind:     by_value
      - .offset:         24
        .size:           4
        .value_kind:     by_value
      - .actual_access:  read_only
        .address_space:  global
        .offset:         32
        .size:           8
        .value_kind:     global_buffer
      - .actual_access:  write_only
        .address_space:  global
        .offset:         40
        .size:           8
        .value_kind:     global_buffer
      - .actual_access:  read_only
        .address_space:  global
        .offset:         48
        .size:           8
        .value_kind:     global_buffer
    .group_segment_fixed_size: 0
    .kernarg_segment_align: 8
    .kernarg_segment_size: 56
    .language:       OpenCL C
    .language_version:
      - 2
      - 0
    .max_flat_workgroup_size: 512
    .name:           _Z11gemm_kernelILi128ELi128ELi4ELi2ELi8ELi1ELi4ELi1EEvPKDF16_S1_iiiPDF16_PfPK15HIP_vector_typeIfLj2EE
    .private_segment_fixed_size: 0
    .sgpr_count:     31
    .sgpr_spill_count: 0
    .symbol:         _Z11gemm_kernelILi128ELi128ELi4ELi2ELi8ELi1ELi4ELi1EEvPKDF16_S1_iiiPDF16_PfPK15HIP_vector_typeIfLj2EE.kd
    .uniform_work_group_size: 1
    .uses_dynamic_stack: false
    .vgpr_count:     62
    .vgpr_spill_count: 0
    .wavefront_size: 64
